# moe_gu unit loop: removed the compiler's s_waitcnt vmcnt(0) at the unit head (gather-list loads, epilogue stores drained before every K-loop); counted vmcnt(6) placed where the list entries are consum
# speedup vs baseline: 1.0168x; 1.0001x over previous
.LBB0_1553:
	s_add_u32 s22, s22, 0x80
	s_addc_u32 s23, s23, 0
	s_add_u32 s2, s24, 0x100
	v_mov_b32_e32 v169, v173
	v_mov_b32_e32 v175, v173
	s_addc_u32 s3, s25, 0
	s_mov_b32 s64, -2
	v_mov_b32_e32 v218, v2
	v_mov_b32_e32 v217, v4
	v_mov_b32_e32 v216, v3
	v_mov_b32_e32 v215, v1
	v_mov_b64_e32 v[32:33], 0
	v_mov_b64_e32 v[34:35], 0
	v_mov_b64_e32 v[36:37], 0
	v_mov_b64_e32 v[38:39], 0
	v_mov_b64_e32 v[40:41], 0
	v_mov_b64_e32 v[42:43], 0
	v_mov_b64_e32 v[44:45], 0
	v_mov_b64_e32 v[46:47], 0
	v_mov_b64_e32 v[48:49], 0
	v_mov_b64_e32 v[50:51], 0
	v_mov_b64_e32 v[52:53], 0
	v_mov_b64_e32 v[54:55], 0
	v_mov_b64_e32 v[56:57], 0
	v_mov_b64_e32 v[58:59], 0
	v_mov_b64_e32 v[60:61], 0
	v_mov_b64_e32 v[62:63], 0
	v_mov_b64_e32 v[64:65], 0
	v_mov_b64_e32 v[66:67], 0
	v_mov_b64_e32 v[68:69], 0
	v_mov_b64_e32 v[70:71], 0
	v_mov_b64_e32 v[72:73], 0
	v_mov_b64_e32 v[74:75], 0
	v_mov_b64_e32 v[76:77], 0
	v_mov_b64_e32 v[78:79], 0
	v_mov_b64_e32 v[80:81], 0
	v_mov_b64_e32 v[82:83], 0
	v_mov_b64_e32 v[84:85], 0
	v_mov_b64_e32 v[86:87], 0
	v_mov_b64_e32 v[88:89], 0
	v_mov_b64_e32 v[90:91], 0
	v_mov_b64_e32 v[92:93], 0
	v_mov_b64_e32 v[94:95], 0
	v_mov_b64_e32 v[96:97], 0
	v_mov_b64_e32 v[98:99], 0
	v_mov_b64_e32 v[100:101], 0
	v_mov_b64_e32 v[102:103], 0
	v_mov_b64_e32 v[104:105], 0
	v_mov_b64_e32 v[106:107], 0
	v_mov_b64_e32 v[108:109], 0
	v_mov_b64_e32 v[110:111], 0
	v_mov_b64_e32 v[112:113], 0
	v_mov_b64_e32 v[114:115], 0
	v_mov_b64_e32 v[116:117], 0
	v_mov_b64_e32 v[118:119], 0
	v_mov_b64_e32 v[120:121], 0
	v_mov_b64_e32 v[122:123], 0
	v_mov_b64_e32 v[124:125], 0
	v_mov_b64_e32 v[126:127], 0
	v_mov_b64_e32 v[128:129], 0
	v_mov_b64_e32 v[130:131], 0
	v_mov_b64_e32 v[132:133], 0
	v_mov_b64_e32 v[134:135], 0
	v_mov_b64_e32 v[136:137], 0
	v_mov_b64_e32 v[138:139], 0
	v_mov_b64_e32 v[140:141], 0
	v_mov_b64_e32 v[142:143], 0
	v_mov_b64_e32 v[144:145], 0
	v_mov_b64_e32 v[146:147], 0
	v_mov_b64_e32 v[148:149], 0
	v_mov_b64_e32 v[150:151], 0
	v_mov_b64_e32 v[152:153], 0
	v_mov_b64_e32 v[154:155], 0
	v_mov_b64_e32 v[156:157], 0
	v_mov_b64_e32 v[158:159], 0
	s_branch .LBB0_1556

.LBB0_1556:
	s_cmp_eq_u32 s64, 4
	s_cselect_b64 s[24:25], -1, 0
	s_cmp_lg_u32 s64, 4
	s_cbranch_scc1 .LBB0_1554
	s_andn2_b64 vcc, exec, s[20:21]
	s_cbranch_vccnz .LBB0_1559
	v_mov_b32_e32 v0, v188
	s_nop 0
	v_ashrrev_i32_e32 v2, 31, v0
	v_lshrrev_b32_e32 v2, 26, v2
	v_lshlrev_b32_e32 v1, 4, v0
	v_add_u32_e32 v2, v0, v2
	v_bfe_i32 v0, v0, 27, 1
	v_lshrrev_b32_e32 v0, 22, v0
	v_add_u32_e32 v0, v1, v0
	v_and_b32_e32 v0, 0xfffffc00, v0
	v_sub_u32_e32 v0, v1, v0
	v_lshrrev_b32_e32 v3, 4, v0
	v_bitop3_b32 v0, v3, v0, 32 bitop3:0x6c
	v_ashrrev_i32_e32 v4, 31, v0
	v_lshrrev_b32_e32 v4, 26, v4
	v_add_u32_e32 v4, v0, v4
	v_ashrrev_i32_e32 v2, 6, v2
	v_ashrrev_i32_e32 v5, 6, v4
	v_and_b32_e32 v4, 0xc0, v4
	v_lshlrev_b32_e32 v3, 3, v2
	v_sub_u32_e32 v0, v0, v4
	v_and_b32_e32 v3, -16, v3
	v_lshlrev_b32_e32 v2, 5, v2
	v_ashrrev_i16_sdwa v0, v201, sext(v0) dst_sel:DWORD dst_unused:UNUSED_PAD src0_sel:DWORD src1_sel:BYTE_0
	v_add_u32_e32 v3, v5, v3
	v_and_b32_e32 v2, 32, v2
	v_bfe_i32 v0, v0, 0, 16
	v_add_lshl_u32 v0, v2, v0, 1
	s_waitcnt vmcnt(6)
	v_lshlrev_b32_e32 v2, 10, v165
	v_cmp_lt_i32_e32 vcc, v3, v222
	s_nop 1
	v_cndmask_b32_e32 v2, 0, v2, vcc
	v_add_u32_e32 v215, v0, v2
	v_add_u32_e32 v2, 0x80, v3
	v_lshlrev_b32_e32 v3, 10, v221
	v_cmp_lt_i32_e32 vcc, v2, v222
	s_nop 1
	v_cndmask_b32_e32 v2, 0, v3, vcc
	v_add_u32_e32 v216, v0, v2
	v_add_u32_e32 v0, 0x2000, v1
	v_ashrrev_i32_e32 v1, 31, v0
	v_lshrrev_b32_e32 v1, 22, v1
	v_add_u32_e32 v1, v0, v1
	v_ashrrev_i32_e32 v1, 10, v1
	v_mul_i32_i24_e32 v2, 0x400, v1
	v_sub_u32_e32 v0, v0, v2
	v_lshrrev_b32_e32 v2, 4, v0
	v_bitop3_b32 v0, v2, v0, 32 bitop3:0x6c
	v_ashrrev_i32_e32 v3, 31, v0
	v_lshrrev_b32_e32 v3, 26, v3
	v_add_u32_e32 v3, v0, v3
	v_ashrrev_i32_e32 v4, 6, v3
	v_and_b32_e32 v3, 0xc0, v3
	v_lshlrev_b32_e32 v2, 3, v1
	v_sub_u32_e32 v0, v0, v3
	v_and_b32_e32 v2, -16, v2
	v_lshlrev_b32_e32 v1, 5, v1
	v_ashrrev_i16_sdwa v0, v201, sext(v0) dst_sel:DWORD dst_unused:UNUSED_PAD src0_sel:DWORD src1_sel:BYTE_0
	v_add_u32_e32 v2, v4, v2
	v_and_b32_e32 v1, 32, v1
	v_bfe_i32 v0, v0, 0, 16
	v_add_lshl_u32 v0, v1, v0, 1
	v_lshlrev_b32_e32 v1, 10, v223
	v_cmp_lt_i32_e32 vcc, v2, v222
	s_nop 1
	v_cndmask_b32_e32 v1, 0, v1, vcc
	v_add_u32_e32 v217, v0, v1
	v_add_u32_e32 v1, 0x80, v2
	v_lshlrev_b32_e32 v2, 10, v224
	v_cmp_lt_i32_e32 vcc, v1, v222
	s_nop 1
	v_cndmask_b32_e32 v1, 0, v2, vcc
	v_add_u32_e32 v218, v0, v1
